# baseline (speedup 1.0000x reference)
.LBB0_118:
	s_or_b64 exec, exec, s[60:61]
	v_readfirstlane_b32 s74, v0
	v_mov_b32_e32 v36, 0x26d50
	ds_read_b128 v[42:45], v36
	s_lshr_b32 s74, s74, 6
	s_and_b32 s74, s74, 3
	s_waitcnt lgkmcnt(0)
	v_readfirstlane_b32 s94, v42
	v_readfirstlane_b32 s95, v43
	v_readfirstlane_b32 s96, v44
	v_readfirstlane_b32 s97, v45
	s_lshl_b32 s94, s94, 2
	s_lshl_b32 s95, s95, 2
	s_lshl_b32 s96, s96, 2
	s_lshl_b32 s97, s97, 2
	s_sub_i32 s98, 0, s74
	s_and_b32 s98, s98, 3
	s_or_b32 s94, s94, s98
	s_sub_i32 s98, 1, s74
	s_and_b32 s98, s98, 3
	s_or_b32 s95, s95, s98
	s_sub_i32 s98, 2, s74
	s_and_b32 s98, s98, 3
	s_or_b32 s96, s96, s98
	s_sub_i32 s98, 3, s74
	s_and_b32 s98, s98, 3
	s_or_b32 s97, s97, s98
	s_min_u32 s94, s94, s95
	s_min_u32 s96, s96, s97
	s_min_u32 s94, s94, s96
	s_and_b32 s94, s94, 3
	s_add_i32 s74, s74, s94
	s_and_b32 s74, s74, 3
	v_mov_b32_e32 v42, 0
	v_mov_b32_e32 v50, 0
	v_mov_b32_e32 v36, s74
	v_lshl_or_b32 v44, v36, 13, v86
	v_mov_b32_e32 v45, 0
	v_lshl_add_u64 v[18:19], s[56:57], 0, v[44:45]
	v_add_co_u32_e32 v34, vcc, 0x1000, v18
	global_load_dwordx4 v[2:5], v44, s[56:57]
	global_load_dwordx4 v[6:9], v44, s[56:57] offset:1024
	global_load_dwordx4 v[10:13], v44, s[56:57] offset:2048
	global_load_dwordx4 v[14:17], v44, s[56:57] offset:3072
	v_addc_co_u32_e32 v35, vcc, 0, v19, vcc
	v_lshlrev_b32_e32 v44, 7, v36
	global_load_dwordx4 v[18:21], v[34:35], off
	global_load_dwordx4 v[22:25], v[34:35], off offset:1024
	global_load_dwordx4 v[26:29], v[34:35], off offset:2048
	global_load_dwordx4 v[30:33], v[34:35], off offset:3072
	v_lshl_add_u64 v[34:35], s[52:53], 0, v[44:45]
	v_lshlrev_b32_e32 v36, 2, v1
	v_mov_b32_e32 v37, v45
	v_lshl_add_u64 v[46:47], v[34:35], 0, v[36:37]
	global_load_dwordx4 v[34:37], v[46:47], off offset:16
	global_load_dwordx4 v[38:41], v[46:47], off
	v_add3_u32 v46, s66, v50, v79
	v_ashrrev_i32_e32 v47, 31, v46
	v_and_b32_e32 v0, 48, v0
	v_lshlrev_b64 v[46:47], 9, v[46:47]
	v_lshlrev_b32_e32 v0, 1, v0
	v_or3_b32 v46, v46, v44, v0
	v_mul_u32_u24_e32 v43, 0x110, v79
	s_movk_i32 s0, 0x1100
	v_lshl_add_u64 v[0:1], s[54:55], 0, v[46:47]
	v_mad_u32_u24 v42, v42, s0, v43
	s_mov_b32 s0, 0x10000
	v_lshl_add_u64 v[0:1], v[0:1], 0, 16
	v_add3_u32 v51, v42, v70, s0
	s_lshl_b32 s75, s74, 2
	s_add_i32 s75, s75, 0x26d50
	s_add_i32 s76, s33, 15
	s_lshr_b32 s76, s76, 4
	v_mov_b64_e32 v[60:61], v[0:1]
	v_mov_b32_e32 v62, v51
	s_mov_b32 s96, 1
